# speedup vs baseline: 1.0019x; 1.0019x over previous
.LBB2_382:
	ds_read_b128 v[152:155], v151
	ds_read_b128 v[156:159], v151 offset:1024
	ds_read_b128 v[164:167], v151 offset:2048
	ds_read_b128 v[168:171], v151 offset:3072
	s_lshl_b32 s58, s84, 7
	s_add_u32 s59, s24, s58
	s_addc_u32 s91, s25, 0
	s_add_u32 s92, s59, 0x80
	s_addc_u32 s93, s91, 0
	s_add_i32 s56, s52, 0xc000
	s_mov_b32 m0, s56
	s_add_i32 s33, s52, 0xe000
	ds_read_b128 v[172:175], v147
	ds_read_b128 v[176:179], v147 offset:1024
	ds_read_b128 v[184:187], v146
	ds_read_b128 v[188:191], v146 offset:1024
	ds_read_b128 v[192:195], v145
	ds_read_b128 v[196:199], v145 offset:1024
	ds_read_b128 v[200:203], v144
	ds_read_b128 v[204:207], v144 offset:1024
	global_load_lds_dwordx4 v132, s[92:93]
	s_mov_b32 m0, s33
	s_nop 0
	global_load_lds_dwordx4 v130, s[92:93]
	s_waitcnt lgkmcnt(8)
	s_barrier
	s_waitcnt lgkmcnt(0)
	v_mfma_f32_16x16x32_f16 v[126:129], v[152:155], v[172:175], v[126:129]
	v_mfma_f32_16x16x32_f16 v[122:125], v[164:167], v[172:175], v[122:125]
	v_mfma_f32_16x16x32_f16 v[118:121], v[152:155], v[184:187], v[118:121]
	v_mfma_f32_16x16x32_f16 v[114:117], v[164:167], v[184:187], v[114:117]
	v_mfma_f32_16x16x32_f16 v[110:113], v[152:155], v[192:195], v[110:113]
	v_mfma_f32_16x16x32_f16 v[106:109], v[164:167], v[192:195], v[106:109]
	v_mfma_f32_16x16x32_f16 v[102:105], v[152:155], v[200:203], v[102:105]
	v_mfma_f32_16x16x32_f16 v[98:101], v[164:167], v[200:203], v[98:101]
	v_mfma_f32_16x16x32_f16 v[126:129], v[156:159], v[176:179], v[126:129]
	v_mfma_f32_16x16x32_f16 v[122:125], v[168:171], v[176:179], v[122:125]
	v_mfma_f32_16x16x32_f16 v[118:121], v[156:159], v[188:191], v[118:121]
	v_mfma_f32_16x16x32_f16 v[114:117], v[168:171], v[188:191], v[114:117]
	v_mfma_f32_16x16x32_f16 v[110:113], v[156:159], v[196:199], v[110:113]
	v_mfma_f32_16x16x32_f16 v[106:109], v[168:171], v[196:199], v[106:109]
	v_mfma_f32_16x16x32_f16 v[102:105], v[156:159], v[204:207], v[102:105]
	v_mfma_f32_16x16x32_f16 v[98:101], v[168:171], v[204:207], v[98:101]
	s_barrier
	s_add_i32 s57, s84, 2
	s_lshl_b32 s82, s57, 7
	s_add_u32 s92, s4, s82
	s_addc_u32 s93, s5, 0
	s_mov_b32 m0, s53
	ds_read_b128 v[208:211], v150
	ds_read_b128 v[212:215], v150 offset:1024
	ds_read_b128 v[216:219], v150 offset:2048
	ds_read_b128 v[220:223], v150 offset:3072
	global_load_lds_dwordx4 v162, s[92:93]
	s_mov_b32 m0, s55
	s_add_u32 s92, s92, 0x40000
	s_addc_u32 s93, s93, 0
	global_load_lds_dwordx4 v162, s[92:93]
	s_barrier
	s_waitcnt lgkmcnt(0)
	v_mfma_f32_16x16x32_f16 v[94:97], v[208:211], v[172:175], v[94:97]
	v_mfma_f32_16x16x32_f16 v[90:93], v[216:219], v[172:175], v[90:93]
	v_mfma_f32_16x16x32_f16 v[86:89], v[208:211], v[184:187], v[86:89]
	v_mfma_f32_16x16x32_f16 v[82:85], v[216:219], v[184:187], v[82:85]
	v_mfma_f32_16x16x32_f16 v[78:81], v[208:211], v[192:195], v[78:81]
	v_mfma_f32_16x16x32_f16 v[74:77], v[216:219], v[192:195], v[74:77]
	v_mfma_f32_16x16x32_f16 v[70:73], v[208:211], v[200:203], v[70:73]
	v_mfma_f32_16x16x32_f16 v[66:69], v[216:219], v[200:203], v[66:69]
	v_mfma_f32_16x16x32_f16 v[94:97], v[212:215], v[176:179], v[94:97]
	v_mfma_f32_16x16x32_f16 v[90:93], v[220:223], v[176:179], v[90:93]
	v_mfma_f32_16x16x32_f16 v[86:89], v[212:215], v[188:191], v[86:89]
	v_mfma_f32_16x16x32_f16 v[82:85], v[220:223], v[188:191], v[82:85]
	v_mfma_f32_16x16x32_f16 v[78:81], v[212:215], v[196:199], v[78:81]
	v_mfma_f32_16x16x32_f16 v[74:77], v[220:223], v[196:199], v[74:77]
	v_mfma_f32_16x16x32_f16 v[70:73], v[212:215], v[204:207], v[70:73]
	v_mfma_f32_16x16x32_f16 v[66:69], v[220:223], v[204:207], v[66:69]
	s_add_u32 s92, s24, s82
	s_addc_u32 s93, s25, 0
	s_mov_b32 m0, s52
	s_barrier
	ds_read_b128 v[172:175], v147 offset:16384
	ds_read_b128 v[176:179], v147 offset:17408
	ds_read_b128 v[184:187], v146 offset:16384
	ds_read_b128 v[188:191], v146 offset:17408
	ds_read_b128 v[192:195], v145 offset:16384
	ds_read_b128 v[196:199], v145 offset:17408
	ds_read_b128 v[200:203], v144 offset:16384
	ds_read_b128 v[204:207], v144 offset:17408
	global_load_lds_dwordx4 v134, s[92:93]
	s_mov_b32 m0, s86
	s_nop 0
	global_load_lds_dwordx4 v136, s[92:93]
	s_barrier
	s_waitcnt lgkmcnt(0)
	v_mfma_f32_16x16x32_f16 v[62:65], v[152:155], v[172:175], v[62:65]
	v_mfma_f32_16x16x32_f16 v[58:61], v[164:167], v[172:175], v[58:61]
	v_mfma_f32_16x16x32_f16 v[54:57], v[152:155], v[184:187], v[54:57]
	v_mfma_f32_16x16x32_f16 v[50:53], v[164:167], v[184:187], v[50:53]
	v_mfma_f32_16x16x32_f16 v[46:49], v[152:155], v[192:195], v[46:49]
	v_mfma_f32_16x16x32_f16 v[42:45], v[164:167], v[192:195], v[42:45]
	v_mfma_f32_16x16x32_f16 v[38:41], v[152:155], v[200:203], v[38:41]
	v_mfma_f32_16x16x32_f16 v[34:37], v[164:167], v[200:203], v[34:37]
	v_mfma_f32_16x16x32_f16 v[62:65], v[156:159], v[176:179], v[62:65]
	v_mfma_f32_16x16x32_f16 v[58:61], v[168:171], v[176:179], v[58:61]
	v_mfma_f32_16x16x32_f16 v[54:57], v[156:159], v[188:191], v[54:57]
	v_mfma_f32_16x16x32_f16 v[50:53], v[168:171], v[188:191], v[50:53]
	v_mfma_f32_16x16x32_f16 v[46:49], v[156:159], v[196:199], v[46:49]
	v_mfma_f32_16x16x32_f16 v[42:45], v[168:171], v[196:199], v[42:45]
	v_mfma_f32_16x16x32_f16 v[38:41], v[156:159], v[204:207], v[38:41]
	v_mfma_f32_16x16x32_f16 v[34:37], v[168:171], v[204:207], v[34:37]
	s_barrier
	s_add_u32 s94, s10, s82
	s_addc_u32 s95, s11, 0
	s_mov_b32 m0, s87
	s_nop 0
	global_load_lds_dwordx4 v162, s[94:95]
	s_mov_b32 m0, s88
	s_add_u32 s94, s94, 0x40000
	s_addc_u32 s95, s95, 0
	global_load_lds_dwordx4 v162, s[94:95]
	s_waitcnt vmcnt(6)
	s_barrier
	v_mfma_f32_16x16x32_f16 v[30:33], v[208:211], v[172:175], v[30:33]
	v_mfma_f32_16x16x32_f16 v[26:29], v[216:219], v[172:175], v[26:29]
	s_mov_b32 m0, s89
	v_mfma_f32_16x16x32_f16 v[22:25], v[208:211], v[184:187], v[22:25]
	global_load_lds_dwordx4 v132, s[92:93]
	v_mfma_f32_16x16x32_f16 v[18:21], v[216:219], v[184:187], v[18:21]
	s_mov_b32 m0, s90
	v_mfma_f32_16x16x32_f16 v[14:17], v[208:211], v[192:195], v[14:17]
	global_load_lds_dwordx4 v130, s[92:93]
	v_mfma_f32_16x16x32_f16 v[10:13], v[216:219], v[192:195], v[10:13]
	v_mfma_f32_16x16x32_f16 v[6:9], v[208:211], v[200:203], v[6:9]
	v_mfma_f32_16x16x32_f16 v[2:5], v[216:219], v[200:203], v[2:5]
	v_mfma_f32_16x16x32_f16 v[30:33], v[212:215], v[176:179], v[30:33]
	v_mfma_f32_16x16x32_f16 v[26:29], v[220:223], v[176:179], v[26:29]
	v_mfma_f32_16x16x32_f16 v[22:25], v[212:215], v[188:191], v[22:25]
	v_mfma_f32_16x16x32_f16 v[18:21], v[220:223], v[188:191], v[18:21]
	v_mfma_f32_16x16x32_f16 v[14:17], v[212:215], v[196:199], v[14:17]
	v_mfma_f32_16x16x32_f16 v[10:13], v[220:223], v[196:199], v[10:13]
	v_mfma_f32_16x16x32_f16 v[6:9], v[212:215], v[204:207], v[6:9]
	v_mfma_f32_16x16x32_f16 v[2:5], v[220:223], v[204:207], v[2:5]
	s_barrier
	ds_read_b128 v[152:155], v149
	ds_read_b128 v[156:159], v149 offset:1024
	ds_read_b128 v[164:167], v149 offset:2048
	ds_read_b128 v[168:171], v149 offset:3072
	ds_read_b128 v[172:175], v147 offset:32768
	ds_read_b128 v[176:179], v147 offset:33792
	ds_read_b128 v[184:187], v146 offset:32768
	ds_read_b128 v[188:191], v146 offset:33792
	ds_read_b128 v[192:195], v145 offset:32768
	ds_read_b128 v[196:199], v145 offset:33792
	ds_read_b128 v[200:203], v144 offset:32768
	ds_read_b128 v[204:207], v144 offset:33792
	s_waitcnt lgkmcnt(8)
	s_barrier
	s_waitcnt lgkmcnt(0)
	v_mfma_f32_16x16x32_f16 v[126:129], v[152:155], v[172:175], v[126:129]
	v_mfma_f32_16x16x32_f16 v[122:125], v[164:167], v[172:175], v[122:125]
	v_mfma_f32_16x16x32_f16 v[118:121], v[152:155], v[184:187], v[118:121]
	v_mfma_f32_16x16x32_f16 v[114:117], v[164:167], v[184:187], v[114:117]
	v_mfma_f32_16x16x32_f16 v[110:113], v[152:155], v[192:195], v[110:113]
	v_mfma_f32_16x16x32_f16 v[106:109], v[164:167], v[192:195], v[106:109]
	v_mfma_f32_16x16x32_f16 v[102:105], v[152:155], v[200:203], v[102:105]
	v_mfma_f32_16x16x32_f16 v[98:101], v[164:167], v[200:203], v[98:101]
	v_mfma_f32_16x16x32_f16 v[126:129], v[156:159], v[176:179], v[126:129]
	v_mfma_f32_16x16x32_f16 v[122:125], v[168:171], v[176:179], v[122:125]
	v_mfma_f32_16x16x32_f16 v[118:121], v[156:159], v[188:191], v[118:121]
	v_mfma_f32_16x16x32_f16 v[114:117], v[168:171], v[188:191], v[114:117]
	v_mfma_f32_16x16x32_f16 v[110:113], v[156:159], v[196:199], v[110:113]
	v_mfma_f32_16x16x32_f16 v[106:109], v[168:171], v[196:199], v[106:109]
	v_mfma_f32_16x16x32_f16 v[102:105], v[156:159], v[204:207], v[102:105]
	v_mfma_f32_16x16x32_f16 v[98:101], v[168:171], v[204:207], v[98:101]
	s_barrier
	s_add_u32 s82, s4, s58
	s_addc_u32 s83, s5, 0
	s_add_u32 s92, s82, 0x180
	s_addc_u32 s93, s83, 0
	s_add_i32 m0, s52, 0x18000
	ds_read_b128 v[208:211], v148
	ds_read_b128 v[212:215], v148 offset:1024
	ds_read_b128 v[216:219], v148 offset:2048
	ds_read_b128 v[220:223], v148 offset:3072
	global_load_lds_dwordx4 v162, s[92:93]
	s_add_i32 m0, s52, 0x1a000
	s_add_u32 s92, s92, 0x40000
	s_addc_u32 s93, s93, 0
	global_load_lds_dwordx4 v162, s[92:93]
	s_barrier
	s_waitcnt lgkmcnt(0)
	v_mfma_f32_16x16x32_f16 v[94:97], v[208:211], v[172:175], v[94:97]
	v_mfma_f32_16x16x32_f16 v[90:93], v[216:219], v[172:175], v[90:93]
	v_mfma_f32_16x16x32_f16 v[86:89], v[208:211], v[184:187], v[86:89]
	v_mfma_f32_16x16x32_f16 v[82:85], v[216:219], v[184:187], v[82:85]
	v_mfma_f32_16x16x32_f16 v[78:81], v[208:211], v[192:195], v[78:81]
	v_mfma_f32_16x16x32_f16 v[74:77], v[216:219], v[192:195], v[74:77]
	v_mfma_f32_16x16x32_f16 v[70:73], v[208:211], v[200:203], v[70:73]
	v_mfma_f32_16x16x32_f16 v[66:69], v[216:219], v[200:203], v[66:69]
	v_mfma_f32_16x16x32_f16 v[94:97], v[212:215], v[176:179], v[94:97]
	v_mfma_f32_16x16x32_f16 v[90:93], v[220:223], v[176:179], v[90:93]
	v_mfma_f32_16x16x32_f16 v[86:89], v[212:215], v[188:191], v[86:89]
	v_mfma_f32_16x16x32_f16 v[82:85], v[220:223], v[188:191], v[82:85]
	v_mfma_f32_16x16x32_f16 v[78:81], v[212:215], v[196:199], v[78:81]
	v_mfma_f32_16x16x32_f16 v[74:77], v[220:223], v[196:199], v[74:77]
	v_mfma_f32_16x16x32_f16 v[70:73], v[212:215], v[204:207], v[70:73]
	v_mfma_f32_16x16x32_f16 v[66:69], v[220:223], v[204:207], v[66:69]
	s_add_u32 s92, s59, 0x180
	s_addc_u32 s93, s91, 0
	s_mov_b32 m0, s34
	s_barrier
	ds_read_b128 v[172:175], v147 offset:49152
	ds_read_b128 v[176:179], v147 offset:50176
	ds_read_b128 v[184:187], v146 offset:49152
	ds_read_b128 v[188:191], v146 offset:50176
	ds_read_b128 v[192:195], v145 offset:49152
	ds_read_b128 v[196:199], v145 offset:50176
	ds_read_b128 v[200:203], v144 offset:49152
	ds_read_b128 v[204:207], v144 offset:50176
	global_load_lds_dwordx4 v134, s[92:93]
	s_mov_b32 m0, s35
	s_nop 0
	global_load_lds_dwordx4 v136, s[92:93]
	s_barrier
	s_waitcnt lgkmcnt(0)
	v_mfma_f32_16x16x32_f16 v[62:65], v[152:155], v[172:175], v[62:65]
	v_mfma_f32_16x16x32_f16 v[58:61], v[164:167], v[172:175], v[58:61]
	v_mfma_f32_16x16x32_f16 v[54:57], v[152:155], v[184:187], v[54:57]
	v_mfma_f32_16x16x32_f16 v[50:53], v[164:167], v[184:187], v[50:53]
	v_mfma_f32_16x16x32_f16 v[46:49], v[152:155], v[192:195], v[46:49]
	v_mfma_f32_16x16x32_f16 v[42:45], v[164:167], v[192:195], v[42:45]
	v_mfma_f32_16x16x32_f16 v[38:41], v[152:155], v[200:203], v[38:41]
	v_mfma_f32_16x16x32_f16 v[34:37], v[164:167], v[200:203], v[34:37]
	v_mfma_f32_16x16x32_f16 v[62:65], v[156:159], v[176:179], v[62:65]
	v_mfma_f32_16x16x32_f16 v[58:61], v[168:171], v[176:179], v[58:61]
	v_mfma_f32_16x16x32_f16 v[54:57], v[156:159], v[188:191], v[54:57]
	v_mfma_f32_16x16x32_f16 v[50:53], v[168:171], v[188:191], v[50:53]
	v_mfma_f32_16x16x32_f16 v[46:49], v[156:159], v[196:199], v[46:49]
	v_mfma_f32_16x16x32_f16 v[42:45], v[168:171], v[196:199], v[42:45]
	v_mfma_f32_16x16x32_f16 v[38:41], v[156:159], v[204:207], v[38:41]
	v_mfma_f32_16x16x32_f16 v[34:37], v[168:171], v[204:207], v[34:37]
	s_barrier
	s_add_u32 s58, s10, s58
	s_addc_u32 s59, s11, 0
	s_add_u32 s58, s58, 0x180
	s_addc_u32 s59, s59, 0
	s_add_i32 m0, s52, 0x1c000
	s_nop 0
	global_load_lds_dwordx4 v162, s[58:59]
	s_add_i32 m0, s52, 0x1e000
	s_add_u32 s58, s58, 0x40000
	s_addc_u32 s59, s59, 0
	global_load_lds_dwordx4 v162, s[58:59]
	s_waitcnt vmcnt(6)
	s_barrier
	v_mfma_f32_16x16x32_f16 v[30:33], v[208:211], v[172:175], v[30:33]
	v_mfma_f32_16x16x32_f16 v[26:29], v[216:219], v[172:175], v[26:29]
	v_mfma_f32_16x16x32_f16 v[22:25], v[208:211], v[184:187], v[22:25]
	v_mfma_f32_16x16x32_f16 v[18:21], v[216:219], v[184:187], v[18:21]
	v_mfma_f32_16x16x32_f16 v[14:17], v[208:211], v[192:195], v[14:17]
	v_mfma_f32_16x16x32_f16 v[10:13], v[216:219], v[192:195], v[10:13]
	v_mfma_f32_16x16x32_f16 v[6:9], v[208:211], v[200:203], v[6:9]
	v_mfma_f32_16x16x32_f16 v[2:5], v[216:219], v[200:203], v[2:5]
	v_mfma_f32_16x16x32_f16 v[30:33], v[212:215], v[176:179], v[30:33]
	v_mfma_f32_16x16x32_f16 v[26:29], v[220:223], v[176:179], v[26:29]
	v_mfma_f32_16x16x32_f16 v[22:25], v[212:215], v[188:191], v[22:25]
	v_mfma_f32_16x16x32_f16 v[18:21], v[220:223], v[188:191], v[18:21]
	v_mfma_f32_16x16x32_f16 v[14:17], v[212:215], v[196:199], v[14:17]
	v_mfma_f32_16x16x32_f16 v[10:13], v[220:223], v[196:199], v[10:13]
	v_mfma_f32_16x16x32_f16 v[6:9], v[212:215], v[204:207], v[6:9]
	v_mfma_f32_16x16x32_f16 v[2:5], v[220:223], v[204:207], v[2:5]
	s_cmp_lt_u32 s84, 28
	s_mov_b32 s84, s57
	s_barrier
	s_cbranch_scc1 .LBB2_382
	v_readlane_b32 s4, v244, 8
	v_readlane_b32 s5, v244, 9
	s_mov_b32 m0, s56
	ds_read_b128 v[134:137], v151
	ds_read_b128 v[152:155], v151 offset:1024
	ds_read_b128 v[156:159], v151 offset:2048
	ds_read_b128 v[164:167], v151 offset:3072
	ds_read_b128 v[168:171], v147
	ds_read_b128 v[172:175], v147 offset:1024
	ds_read_b128 v[176:179], v146
	ds_read_b128 v[184:187], v146 offset:1024
	ds_read_b128 v[188:191], v145
	ds_read_b128 v[192:195], v145 offset:1024
	ds_read_b128 v[196:199], v144
	ds_read_b128 v[200:203], v144 offset:1024
	v_lshl_add_u64 v[132:133], s[4:5], 0, v[132:133]
	global_load_lds_dwordx4 v[132:133], off
	v_lshl_add_u64 v[130:131], s[4:5], 0, v[130:131]
	s_mov_b32 m0, s33
	s_nop 0
	global_load_lds_dwordx4 v[130:131], off
	s_barrier
	s_waitcnt lgkmcnt(0)
	v_mfma_f32_16x16x32_f16 v[126:129], v[134:137], v[168:171], v[126:129]
	v_mfma_f32_16x16x32_f16 v[122:125], v[156:159], v[168:171], v[122:125]
	v_mfma_f32_16x16x32_f16 v[110:113], v[134:137], v[188:191], v[110:113]
	v_mfma_f32_16x16x32_f16 v[106:109], v[156:159], v[188:191], v[106:109]
	v_mfma_f32_16x16x32_f16 v[126:129], v[152:155], v[172:175], v[126:129]
	v_mfma_f32_16x16x32_f16 v[122:125], v[164:167], v[172:175], v[122:125]
	v_mfma_f32_16x16x32_f16 v[118:121], v[134:137], v[176:179], v[118:121]
	v_mfma_f32_16x16x32_f16 v[114:117], v[156:159], v[176:179], v[114:117]
	v_mfma_f32_16x16x32_f16 v[110:113], v[152:155], v[192:195], v[110:113]
	v_mfma_f32_16x16x32_f16 v[106:109], v[164:167], v[192:195], v[106:109]
	v_mfma_f32_16x16x32_f16 v[102:105], v[134:137], v[196:199], v[102:105]
	v_mfma_f32_16x16x32_f16 v[98:101], v[156:159], v[196:199], v[98:101]
	v_mfma_f32_16x16x32_f16 v[130:133], v[152:155], v[184:187], v[118:121]
	v_mfma_f32_16x16x32_f16 v[204:207], v[164:167], v[184:187], v[114:117]
	v_mfma_f32_16x16x32_f16 v[208:211], v[152:155], v[200:203], v[102:105]
	v_mfma_f32_16x16x32_f16 v[212:215], v[164:167], v[200:203], v[98:101]
	s_barrier
	s_nop 1
	ds_read_b128 v[98:101], v150
	ds_read_b128 v[102:105], v150 offset:1024
	ds_read_b128 v[114:117], v150 offset:2048
	ds_read_b128 v[118:121], v150 offset:3072
	s_barrier
	s_waitcnt lgkmcnt(0)
	v_mfma_f32_16x16x32_f16 v[94:97], v[98:101], v[168:171], v[94:97]
	v_mfma_f32_16x16x32_f16 v[90:93], v[114:117], v[168:171], v[90:93]
	v_mfma_f32_16x16x32_f16 v[78:81], v[98:101], v[188:191], v[78:81]
	v_mfma_f32_16x16x32_f16 v[74:77], v[114:117], v[188:191], v[74:77]
	v_mfma_f32_16x16x32_f16 v[94:97], v[102:105], v[172:175], v[94:97]
	v_mfma_f32_16x16x32_f16 v[90:93], v[118:121], v[172:175], v[90:93]
	v_mfma_f32_16x16x32_f16 v[86:89], v[98:101], v[176:179], v[86:89]
	v_mfma_f32_16x16x32_f16 v[82:85], v[114:117], v[176:179], v[82:85]
	v_mfma_f32_16x16x32_f16 v[78:81], v[102:105], v[192:195], v[78:81]
	v_mfma_f32_16x16x32_f16 v[74:77], v[118:121], v[192:195], v[74:77]
	v_mfma_f32_16x16x32_f16 v[70:73], v[98:101], v[196:199], v[70:73]
	v_mfma_f32_16x16x32_f16 v[66:69], v[114:117], v[196:199], v[66:69]
	v_mfma_f32_16x16x32_f16 v[168:171], v[102:105], v[184:187], v[86:89]
	v_mfma_f32_16x16x32_f16 v[172:175], v[118:121], v[184:187], v[82:85]
	v_mfma_f32_16x16x32_f16 v[176:179], v[102:105], v[200:203], v[70:73]
	v_mfma_f32_16x16x32_f16 v[184:187], v[118:121], v[200:203], v[66:69]
	s_barrier
	s_nop 1
	ds_read_b128 v[66:69], v147 offset:16384
	ds_read_b128 v[70:73], v147 offset:17408
	ds_read_b128 v[82:85], v146 offset:16384
	ds_read_b128 v[86:89], v146 offset:17408
	ds_read_b128 v[188:191], v145 offset:16384
	ds_read_b128 v[192:195], v145 offset:17408
	ds_read_b128 v[196:199], v144 offset:16384
	ds_read_b128 v[200:203], v144 offset:17408
	s_waitcnt vmcnt(4)
	s_barrier
	s_waitcnt lgkmcnt(0)
	v_mfma_f32_16x16x32_f16 v[62:65], v[134:137], v[66:69], v[62:65]
	v_mfma_f32_16x16x32_f16 v[58:61], v[156:159], v[66:69], v[58:61]
	v_mfma_f32_16x16x32_f16 v[46:49], v[134:137], v[188:191], v[46:49]
	v_mfma_f32_16x16x32_f16 v[42:45], v[156:159], v[188:191], v[42:45]
	v_mfma_f32_16x16x32_f16 v[62:65], v[152:155], v[70:73], v[62:65]
	v_mfma_f32_16x16x32_f16 v[58:61], v[164:167], v[70:73], v[58:61]
	v_mfma_f32_16x16x32_f16 v[54:57], v[134:137], v[82:85], v[54:57]
	v_mfma_f32_16x16x32_f16 v[50:53], v[156:159], v[82:85], v[50:53]
	v_mfma_f32_16x16x32_f16 v[46:49], v[152:155], v[192:195], v[46:49]
	v_mfma_f32_16x16x32_f16 v[42:45], v[164:167], v[192:195], v[42:45]
	v_mfma_f32_16x16x32_f16 v[38:41], v[134:137], v[196:199], v[38:41]
	v_mfma_f32_16x16x32_f16 v[34:37], v[156:159], v[196:199], v[34:37]
	v_mfma_f32_16x16x32_f16 v[216:219], v[152:155], v[86:89], v[54:57]
	v_mfma_f32_16x16x32_f16 v[220:223], v[164:167], v[86:89], v[50:53]
	v_mfma_f32_16x16x32_f16 v[134:137], v[152:155], v[200:203], v[38:41]
	v_mfma_f32_16x16x32_f16 v[150:153], v[164:167], v[200:203], v[34:37]
	v_mfma_f32_16x16x32_f16 v[30:33], v[98:101], v[66:69], v[30:33]
	v_mfma_f32_16x16x32_f16 v[26:29], v[114:117], v[66:69], v[26:29]
	v_mfma_f32_16x16x32_f16 v[14:17], v[98:101], v[188:191], v[14:17]
	v_mfma_f32_16x16x32_f16 v[10:13], v[114:117], v[188:191], v[10:13]
	v_mfma_f32_16x16x32_f16 v[30:33], v[102:105], v[70:73], v[30:33]
	v_mfma_f32_16x16x32_f16 v[26:29], v[118:121], v[70:73], v[26:29]
	v_mfma_f32_16x16x32_f16 v[22:25], v[98:101], v[82:85], v[22:25]
	v_mfma_f32_16x16x32_f16 v[18:21], v[114:117], v[82:85], v[18:21]
	v_mfma_f32_16x16x32_f16 v[14:17], v[102:105], v[192:195], v[14:17]
	v_mfma_f32_16x16x32_f16 v[10:13], v[118:121], v[192:195], v[10:13]
	v_mfma_f32_16x16x32_f16 v[6:9], v[98:101], v[196:199], v[6:9]
	v_mfma_f32_16x16x32_f16 v[2:5], v[114:117], v[196:199], v[2:5]
	v_mfma_f32_16x16x32_f16 v[154:157], v[102:105], v[86:89], v[22:25]
	v_mfma_f32_16x16x32_f16 v[158:161], v[118:121], v[86:89], v[18:21]
	v_mfma_f32_16x16x32_f16 v[164:167], v[102:105], v[200:203], v[6:9]
	v_mfma_f32_16x16x32_f16 v[188:191], v[118:121], v[200:203], v[2:5]
	s_barrier
	s_nop 1
	ds_read_b128 v[2:5], v149
	ds_read_b128 v[6:9], v149 offset:1024
	ds_read_b128 v[192:195], v149 offset:2048
	ds_read_b128 v[196:199], v149 offset:3072
	ds_read_b128 v[18:21], v147 offset:32768
	ds_read_b128 v[22:25], v147 offset:33792
	ds_read_b128 v[34:37], v146 offset:32768
	ds_read_b128 v[38:41], v146 offset:33792
	ds_read_b128 v[50:53], v145 offset:32768
	ds_read_b128 v[54:57], v145 offset:33792
	ds_read_b128 v[200:203], v144 offset:32768
	ds_read_b128 v[224:227], v144 offset:33792
	s_waitcnt vmcnt(2)
	s_barrier
	s_waitcnt lgkmcnt(0)
	v_mfma_f32_16x16x32_f16 v[66:69], v[2:5], v[18:21], v[126:129]
	v_mfma_f32_16x16x32_f16 v[118:121], v[6:9], v[22:25], v[66:69]
	v_mfma_f32_16x16x32_f16 v[66:69], v[192:195], v[18:21], v[122:125]
	v_mfma_f32_16x16x32_f16 v[114:117], v[196:199], v[22:25], v[66:69]
	v_mfma_f32_16x16x32_f16 v[66:69], v[2:5], v[34:37], v[130:133]
	v_mfma_f32_16x16x32_f16 v[102:105], v[6:9], v[38:41], v[66:69]
	v_mfma_f32_16x16x32_f16 v[66:69], v[192:195], v[34:37], v[204:207]
	v_mfma_f32_16x16x32_f16 v[98:101], v[196:199], v[38:41], v[66:69]
	v_mfma_f32_16x16x32_f16 v[66:69], v[2:5], v[50:53], v[110:113]
	v_mfma_f32_16x16x32_f16 v[86:89], v[6:9], v[54:57], v[66:69]
	v_mfma_f32_16x16x32_f16 v[66:69], v[192:195], v[50:53], v[106:109]
	v_mfma_f32_16x16x32_f16 v[82:85], v[196:199], v[54:57], v[66:69]
	v_mfma_f32_16x16x32_f16 v[66:69], v[2:5], v[200:203], v[208:211]
	v_mfma_f32_16x16x32_f16 v[70:73], v[6:9], v[224:227], v[66:69]
	v_mfma_f32_16x16x32_f16 v[66:69], v[192:195], v[200:203], v[212:215]
	v_mfma_f32_16x16x32_f16 v[66:69], v[196:199], v[224:227], v[66:69]
	s_barrier
	ds_read_b128 v[130:133], v148
	ds_read_b128 v[204:207], v148 offset:1024
	ds_read_b128 v[208:211], v148 offset:2048
	ds_read_b128 v[212:215], v148 offset:3072
	s_waitcnt vmcnt(0)
	s_barrier
	s_waitcnt lgkmcnt(0)
	v_mfma_f32_16x16x32_f16 v[94:97], v[130:133], v[18:21], v[94:97]
	v_mfma_f32_16x16x32_f16 v[18:21], v[208:211], v[18:21], v[90:93]
	v_mfma_f32_16x16x32_f16 v[122:125], v[212:215], v[22:25], v[18:21]
	v_mfma_f32_16x16x32_f16 v[18:21], v[130:133], v[34:37], v[168:171]
	v_mfma_f32_16x16x32_f16 v[110:113], v[204:207], v[38:41], v[18:21]
	v_mfma_f32_16x16x32_f16 v[18:21], v[208:211], v[34:37], v[172:175]
	v_mfma_f32_16x16x32_f16 v[106:109], v[212:215], v[38:41], v[18:21]
	v_mfma_f32_16x16x32_f16 v[18:21], v[130:133], v[50:53], v[78:81]
	v_mfma_f32_16x16x32_f16 v[126:129], v[204:207], v[22:25], v[94:97]
	v_mfma_f32_16x16x32_f16 v[94:97], v[204:207], v[54:57], v[18:21]
	v_mfma_f32_16x16x32_f16 v[18:21], v[208:211], v[50:53], v[74:77]
	v_mfma_f32_16x16x32_f16 v[90:93], v[212:215], v[54:57], v[18:21]
	v_mfma_f32_16x16x32_f16 v[18:21], v[130:133], v[200:203], v[176:179]
	v_mfma_f32_16x16x32_f16 v[78:81], v[204:207], v[224:227], v[18:21]
	v_mfma_f32_16x16x32_f16 v[18:21], v[208:211], v[200:203], v[184:187]
	v_mfma_f32_16x16x32_f16 v[74:77], v[212:215], v[224:227], v[18:21]
	s_barrier
	ds_read_b128 v[168:171], v147 offset:49152
	ds_read_b128 v[172:175], v147 offset:50176
	ds_read_b128 v[176:179], v146 offset:49152
	ds_read_b128 v[146:149], v146 offset:50176
	ds_read_b128 v[184:187], v145 offset:49152
	ds_read_b128 v[200:203], v145 offset:50176
	ds_read_b128 v[224:227], v144 offset:49152
	ds_read_b128 v[228:231], v144 offset:50176
	s_barrier
	s_waitcnt lgkmcnt(0)
	v_mfma_f32_16x16x32_f16 v[18:21], v[2:5], v[168:171], v[62:65]
	v_mfma_f32_16x16x32_f16 v[54:57], v[6:9], v[172:175], v[18:21]
	v_mfma_f32_16x16x32_f16 v[18:21], v[192:195], v[168:171], v[58:61]
	v_mfma_f32_16x16x32_f16 v[50:53], v[196:199], v[172:175], v[18:21]
	v_mfma_f32_16x16x32_f16 v[18:21], v[2:5], v[176:179], v[216:219]
	v_mfma_f32_16x16x32_f16 v[38:41], v[6:9], v[146:149], v[18:21]
	v_mfma_f32_16x16x32_f16 v[18:21], v[192:195], v[176:179], v[220:223]
	v_mfma_f32_16x16x32_f16 v[34:37], v[196:199], v[146:149], v[18:21]
	v_mfma_f32_16x16x32_f16 v[18:21], v[2:5], v[184:187], v[46:49]
	v_mfma_f32_16x16x32_f16 v[2:5], v[2:5], v[224:227], v[134:137]
	v_mfma_f32_16x16x32_f16 v[22:25], v[6:9], v[200:203], v[18:21]
	v_mfma_f32_16x16x32_f16 v[18:21], v[192:195], v[184:187], v[42:45]
	v_mfma_f32_16x16x32_f16 v[6:9], v[6:9], v[228:231], v[2:5]
	v_mfma_f32_16x16x32_f16 v[2:5], v[192:195], v[224:227], v[150:153]
	v_mfma_f32_16x16x32_f16 v[18:21], v[196:199], v[200:203], v[18:21]
	v_mfma_f32_16x16x32_f16 v[2:5], v[196:199], v[228:231], v[2:5]
	v_mfma_f32_16x16x32_f16 v[26:29], v[208:211], v[168:171], v[26:29]
	v_mfma_f32_16x16x32_f16 v[58:61], v[212:215], v[172:175], v[26:29]
	v_mfma_f32_16x16x32_f16 v[26:29], v[130:133], v[176:179], v[154:157]
	v_mfma_f32_16x16x32_f16 v[46:49], v[204:207], v[146:149], v[26:29]
	v_mfma_f32_16x16x32_f16 v[26:29], v[208:211], v[176:179], v[158:161]
	v_mfma_f32_16x16x32_f16 v[10:13], v[208:211], v[184:187], v[10:13]
	v_mfma_f32_16x16x32_f16 v[30:33], v[130:133], v[168:171], v[30:33]
	v_mfma_f32_16x16x32_f16 v[42:45], v[212:215], v[146:149], v[26:29]
	v_mfma_f32_16x16x32_f16 v[14:17], v[130:133], v[184:187], v[14:17]
	v_mfma_f32_16x16x32_f16 v[26:29], v[212:215], v[200:203], v[10:13]
	v_mfma_f32_16x16x32_f16 v[10:13], v[130:133], v[224:227], v[164:167]
	v_mfma_f32_16x16x32_f16 v[62:65], v[204:207], v[172:175], v[30:33]
	v_mfma_f32_16x16x32_f16 v[30:33], v[204:207], v[200:203], v[14:17]
	v_mfma_f32_16x16x32_f16 v[14:17], v[204:207], v[228:231], v[10:13]
	v_mfma_f32_16x16x32_f16 v[10:13], v[208:211], v[224:227], v[188:191]
	v_mfma_f32_16x16x32_f16 v[10:13], v[212:215], v[228:231], v[10:13]
